# GDN chain compute: LDS reads issued before previous-step output stores + loader counted waits
# speedup vs baseline: 1.0081x; 1.0081x over previous
; #define MFMA32(a, b, c) __builtin_amdgcn_mfma_f32_16x16x32_bf16((a), (b), (c), 0, 0, 0)
; __device__ __forceinline__ float lo16(unsigned u) { return __uint_as_float(u << 16); }
; __device__ void phase_gdn_chain(const Params& p, int l, char* smem, int vb, int nvb, int oz) {
;     ...
;             for (int ci = 0; ci < 36; ++ci) {
;                 if (ohave) {
; #pragma unroll
;                     for (int mt = 0; mt < 4; ++mt)
;                         *(bf16x4*)(U + (orow + 16 * mt + li) * LDU + C_GQ + dir * 256 + h * 64 + 16 * sl + 4 * g) = ost[mt];
;                 }
;                 const ChunkInfo c = chunk_info<64>(ci, dir, b);
;                 const bool need_o = !c.isctx || with_ctx;
;                 const char* bp = smem + (ci & 1) * BUFB;
;                 const bf16_t* WD = (const bf16_t*)bp;
;                 const bf16_t* AT = WD + 64 * LS;
;                 const bf16_t* KT = AT + 64 * LS;
;                 const bf16_t* QQ = KT + 64 * LS;
;                 const bf16_t* UVl = QQ + 64 * LS;
;                 const float* eG = (const float*)(bp + 4 * TILEB + 8192);
;                 const float* eT = eG + 64;
;                 const float gt = eG[128];
;                 u32x2 uvw[4];
;                 bf16x8 wa[4][2], ka[4][2];
;                 f32x4 e0[2], e1[2];
; #pragma unroll
;                 for (int mt = 0; mt < 4; ++mt) {
;                     uvw[mt] = *(const u32x2*)(UVl + ((mt * 4 + sl) * 64 + lane) * 4);
; #pragma unroll
;                     for (int s = 0; s < 2; ++s) {
;                         wa[mt][s] = *(const bf16x8*)(WD + (16 * mt + li) * LS + 32 * s + 8 * g);
;                     }
;                 }
; #pragma unroll
;                 for (int s = 0; s < 2; ++s) { e0[s] = *(const f32x4*)(eT + 32 * s + 4 * g); e1[s] = *(const f32x4*)(eT + 32 * s + 16 + 4 * g); }
;                 bf16x8 sf[2];
; #pragma unroll
;                 for (int s = 0; s < 2; ++s) sf[s] = pack8(S[2 * s], S[2 * s + 1]);
;                 __builtin_amdgcn_sched_barrier(0);
;                 f32x4 vn[4];
; #pragma unroll
;                 for (int mt = 0; mt < 4; ++mt) {
;                     vn[mt] = (f32x4){lo16(uvw[mt][0]), hi16(uvw[mt][0]), lo16(uvw[mt][1]), hi16(uvw[mt][1])};
; #pragma unroll
;                     for (int s = 0; s < 2; ++s) vn[mt] = MFMA32(wa[mt][s], sf[s], vn[mt]);
;                 }
.LBB0_396:
	v_mov_b32_e32 v164, v90
	v_mov_b32_e32 v165, v91
	v_mov_b32_e32 v166, v88
	v_mov_b32_e32 v167, v89
	v_mov_b32_e32 v168, v86
	v_mov_b32_e32 v169, v87
	v_mov_b32_e32 v170, v84
	v_mov_b32_e32 v171, v85
	s_cmp_gt_u32 s26, 3
	s_cselect_b64 s[56:57], -1, 0
	s_bitcmp1_b32 s26, 0
	s_cselect_b32 s0, 0xb210, 0
	s_add_i32 s0, s0, 0
	v_mov_b32_e32 v2, s0
	v_add3_u32 v84, s0, v203, v205
	ds_read2st64_b64 v[94:97], v84 offset0:72 offset1:76
	v_add3_u32 v172, s0, v191, v207
	ds_read_b32 v2, v2 offset:45568
	ds_read_b128 v[104:107], v172
	ds_read_b128 v[112:115], v172 offset:64
	ds_read_b128 v[124:127], v172 offset:2304
	ds_read2st64_b64 v[128:131], v84 offset0:80 offset1:84
	ds_read_b128 v[132:135], v172 offset:2368
	ds_read_b128 v[136:139], v172 offset:4608
	ds_read_b128 v[140:143], v172 offset:4672
	ds_read_b128 v[144:147], v172 offset:6912
	ds_read_b128 v[174:177], v172 offset:6976
	v_lshl_add_u32 v173, v192, 2, s0
	ds_read_b128 v[120:123], v173 offset:45312
	ds_read_b128 v[116:119], v173 offset:45376
	ds_read_b128 v[108:111], v173 offset:45440
	ds_read_b128 v[100:103], v173 offset:45504
	s_andn2_b64 vcc, exec, s[52:53]
	s_cbranch_vccnz .LBB0_398
	v_mov_b32_e32 v185, 0
	v_lshl_add_u64 v[180:181], s[54:55], 0, v[188:189]
	v_mov_b64_e32 v[182:183], s[34:35]
	v_mad_u64_u32 v[182:183], s[4:5], v180, s92, v[182:183]
	v_mov_b32_e32 v184, v183
	v_mad_u64_u32 v[180:181], s[4:5], v181, s92, v[184:185]
	v_mov_b32_e32 v183, v180
	s_lshl_b32 s96, s81, 1
	v_lshl_add_u64 v[180:181], v[182:183], 0, s[96:97]
	s_lshl_b32 s96, s3, 1
	v_lshl_add_u64 v[180:181], v[180:181], 0, s[96:97]
	v_lshlrev_b32_e32 v184, 1, v194
	v_lshl_add_u64 v[180:181], v[180:181], 0, v[184:185]
	v_lshlrev_b32_e32 v184, 1, v192
	v_lshl_add_u64 v[180:181], v[180:181], 0, v[184:185]
	v_add_co_u32_e32 v182, vcc, 0x1a000, v180
	global_store_dwordx2 v[180:181], v[164:165], off offset:1024
	s_nop 0
	v_addc_co_u32_e32 v183, vcc, 0, v181, vcc
	global_store_dwordx2 v[182:183], v[166:167], off offset:3072
	v_add_co_u32_e32 v182, vcc, 0x35000, v180
	s_nop 1
	v_addc_co_u32_e32 v183, vcc, 0, v181, vcc
	v_add_co_u32_e32 v180, vcc, 0x4f000, v180
	global_store_dwordx2 v[182:183], v[168:169], off offset:1024
	s_nop 0
	v_addc_co_u32_e32 v181, vcc, 0, v181, vcc
	global_store_dwordx2 v[180:181], v[170:171], off offset:3072
.LBB0_398:
	s_or_b64 s[52:53], s[20:21], s[56:57]
	v_cvt_pk_bf16_f32 v84, v80, v81
	v_cvt_pk_bf16_f32 v85, v82, v83
	v_cvt_pk_bf16_f32 v86, v76, v77
	v_cvt_pk_bf16_f32 v87, v78, v79
	v_cvt_pk_bf16_f32 v88, v72, v73
	v_cvt_pk_bf16_f32 v89, v74, v75
	v_cvt_pk_bf16_f32 v90, v68, v69
	v_cvt_pk_bf16_f32 v91, v70, v71
	s_waitcnt lgkmcnt(0)
	v_lshlrev_b32_e32 v92, 16, v94
	v_and_b32_e32 v93, 0xffff0000, v94
	v_lshlrev_b32_e32 v94, 16, v95
	v_and_b32_e32 v95, 0xffff0000, v95
	ds_read_b128 v[152:155], v172 offset:18432
	ds_read_b128 v[148:151], v172 offset:18496
	v_mfma_f32_16x16x32_bf16 v[92:95], v[104:107], v[84:87], v[92:95]
	v_lshlrev_b32_e32 v104, 16, v96
	v_and_b32_e32 v105, 0xffff0000, v96
	v_lshlrev_b32_e32 v106, 16, v97
	v_and_b32_e32 v107, 0xffff0000, v97
	v_mfma_f32_16x16x32_bf16 v[92:95], v[112:115], v[88:91], v[92:95]
	v_lshlrev_b32_e32 v112, 16, v130
	v_and_b32_e32 v113, 0xffff0000, v130
	v_lshlrev_b32_e32 v114, 16, v131
	v_mfma_f32_16x16x32_bf16 v[96:99], v[124:127], v[84:87], v[104:107]
	v_and_b32_e32 v115, 0xffff0000, v131
	s_andn2_b64 vcc, exec, s[52:53]
	s_nop 0
	v_lshlrev_b32_e32 v104, 16, v128
	v_and_b32_e32 v105, 0xffff0000, v128
	v_lshlrev_b32_e32 v106, 16, v129
	v_and_b32_e32 v107, 0xffff0000, v129
	v_mfma_f32_16x16x32_bf16 v[112:115], v[144:147], v[84:87], v[112:115]
	s_nop 0
	v_mfma_f32_16x16x32_bf16 v[104:107], v[136:139], v[84:87], v[104:107]
	v_mfma_f32_16x16x32_bf16 v[96:99], v[132:135], v[88:91], v[96:99]
	v_mfma_f32_16x16x32_bf16 v[104:107], v[140:143], v[88:91], v[104:107]
	ds_read_b128 v[140:143], v172 offset:20736
	ds_read_b128 v[144:147], v172 offset:20800
	ds_read_b128 v[132:135], v172 offset:23040
	ds_read_b128 v[136:139], v172 offset:23104
	ds_read_b128 v[128:131], v172 offset:25344
	ds_read_b128 v[124:127], v172 offset:25408
	v_cndmask_b32_e64 v172, 0, 1, s[52:53]
	v_mfma_f32_16x16x32_bf16 v[112:115], v[174:177], v[88:91], v[112:115]
	v_cmp_ne_u32_e64 s[42:43], 1, v172
	v_cndmask_b32_e64 v172, 0, 1, s[28:29]
	s_cbranch_vccnz .LBB0_408
	v_lshl_add_u32 v52, v188, 2, s0
	v_lshl_add_u32 v64, v209, 1, v173
	ds_read_b32 v206, v52 offset:45056
	ds_read_b128 v[28:31], v64 offset:9216
	ds_read_b128 v[20:23], v64 offset:27648
	ds_read_b128 v[16:19], v64 offset:27712
	v_cmp_ne_u32_e64 s[0:1], 1, v172
	s_andn2_b64 vcc, exec, s[28:29]
	s_cbranch_vccnz .LBB0_401
	ds_read_b128 v[24:27], v64 offset:9280
